# moe2: weights of K tile 2 loaded with the unit's prefetch into spare registers (moved into place at the start of the K loop)
# baseline (speedup 1.0000x reference)
; #define G_LOAD(SA, SB, KT) do { SA.load(al, (KT) * 32); SB.load(bl, (KT) * 32); } while (0)
;     __device__ __forceinline__ void prefetch(const AL& al, const BL& bl) {
;         G_LOAD(sa0, sb0, 0);
;         if (1 < nk) G_LOAD(sa1, sb1, 1);
;         if constexpr (BL::DEPTH == 3) { if (2 < nk) G_LOAD(sa2, sb2, 2); }
.LBB0_1562:
	s_or_b64 exec, exec, s[6:7]
	v_add_co_u32_e32 v2, vcc, 0x20000, v214
	s_add_i32 s26, 0, 0x21290
	s_nop 0
	v_addc_co_u32_e32 v3, vcc, 0, v215, vcc
	v_add_co_u32_e32 v4, vcc, 0x21000, v214
	s_add_i32 s25, 0, 0x21950
	s_nop 0
	v_addc_co_u32_e32 v5, vcc, 0, v215, vcc
	global_load_dwordx4 v[130:133], v[2:3], off
	global_load_dwordx4 v[134:137], v[4:5], off
	v_add_co_u32_e32 v2, vcc, 0x22000, v214
	s_nop 1
	v_addc_co_u32_e32 v3, vcc, 0, v215, vcc
	v_add_co_u32_e32 v4, vcc, 0x23000, v214
	s_nop 1
	v_addc_co_u32_e32 v5, vcc, 0, v215, vcc
	global_load_dwordx4 v[138:141], v[2:3], off
	global_load_dwordx4 v[142:145], v[4:5], off
	v_add_co_u32_e32 v234, vcc, 0x40000, v214
	s_nop 1
	v_addc_co_u32_e32 v235, vcc, 0, v215, vcc
	global_load_dwordx4 v[236:239], v[234:235], off
	v_add_co_u32_e32 v234, vcc, 0x41000, v214
	s_nop 1
	v_addc_co_u32_e32 v235, vcc, 0, v215, vcc
	global_load_dwordx4 v[240:243], v[234:235], off
	v_add_co_u32_e32 v234, vcc, 0x42000, v214
	s_nop 1
	v_addc_co_u32_e32 v235, vcc, 0, v215, vcc
	global_load_dwordx4 v[244:247], v[234:235], off
	v_add_co_u32_e32 v234, vcc, 0x43000, v214
	s_nop 1
	v_addc_co_u32_e32 v235, vcc, 0, v215, vcc
	global_load_dwordx4 v[248:251], v[234:235], off
	s_andn2_b64 vcc, exec, s[4:5]
	s_cbranch_vccnz .LBB0_1626

; #define G_LOAD(SA, SB, KT) do { SA.load(al, (KT) * 32); SB.load(bl, (KT) * 32); } while (0)
; #define G_STORE(SA, SB, BUF) do { SA.store(As + (BUF) * ASZ, tid); SB.store(Bs3 + (BUF) * BSZ, tid); } while (0)
;     __device__ __forceinline__ void mainloop(bfr* smem, const AL& al, const BL& bl) {
;     ...
;         __syncthreads();
;         G_STORE(sa0, sb0, 0);
;         if (1 < nk) G_STORE(sa1, sb1, 1);
;         if (BL::DEPTH < nk) G_LOAD(sa0, sb0, BL::DEPTH);
;         if (BL::DEPTH + 1 < nk) G_LOAD(sa1, sb1, BL::DEPTH + 1);
;         __builtin_amdgcn_sched_barrier(0);
.LBB0_1571:
	s_or_b64 exec, exec, s[12:13]
	v_add_co_u32_e32 v2, vcc, 0x40000, v214
	s_nop 1
	v_addc_co_u32_e32 v3, vcc, 0, v215, vcc
	v_add_co_u32_e32 v4, vcc, 0x41000, v214
	s_nop 1
	v_addc_co_u32_e32 v5, vcc, 0, v215, vcc
	v_mov_b64_e32 v[134:135], v[236:237]
	v_mov_b64_e32 v[136:137], v[238:239]
	v_mov_b64_e32 v[122:123], v[240:241]
	v_mov_b64_e32 v[124:125], v[242:243]
	v_add_co_u32_e32 v2, vcc, 0x42000, v214
	s_nop 1
	v_addc_co_u32_e32 v3, vcc, 0, v215, vcc
	v_add_co_u32_e32 v4, vcc, 0x43000, v214
	s_nop 1
	v_addc_co_u32_e32 v5, vcc, 0, v215, vcc
	v_mov_b64_e32 v[150:151], v[244:245]
	v_mov_b64_e32 v[152:153], v[246:247]
	v_mov_b64_e32 v[142:143], v[248:249]
	v_mov_b64_e32 v[144:145], v[250:251]
	global_load_dwordx4 v[110:113], v[200:201], off offset:192
	s_and_saveexec_b64 s[12:13], s[4:5]
	s_cbranch_execz .LBB0_1573
	global_load_dwordx4 v[102:105], v[206:207], off offset:192

.Lm2a_ld_8:
	global_load_dword v234, v[248:249], off
	ds_read_b64_tr_b16 v[2:3], v232 offset:46096
	ds_read_b64_tr_b16 v[4:5], v232 offset:48400
	ds_read_b64_tr_b16 v[8:9], v232 offset:48464
	ds_read_b64_tr_b16 v[6:7], v232 offset:46160
	ds_read_b128 v[10:13], v219 offset:16
	ds_read_b128 v[146:149], v219 offset:48
	ds_read_b128 v[14:17], v219 offset:2576
	ds_read_b128 v[158:161], v219 offset:2608
	ds_read_b128 v[138:141], v219 offset:5136
	ds_read_b128 v[162:165], v219 offset:5168
	ds_read_b64_tr_b16 v[182:183], v232 offset:55312
	ds_read_b64_tr_b16 v[184:185], v232 offset:57616
	ds_read_b64_tr_b16 v[180:181], v232 offset:57680
	ds_read_b64_tr_b16 v[178:179], v232 offset:55376
	s_waitcnt lgkmcnt(9)
	v_mfma_f32_32x32x16_bf16 v[82:97], v[10:13], v[2:5], 0
	v_mfma_f32_32x32x16_bf16 v[66:81], v[10:13], v[6:9], 0
	ds_read_b128 v[166:169], v219 offset:15376
	s_waitcnt lgkmcnt(8)
	v_mfma_f32_32x32x16_bf16 v[50:65], v[14:17], v[2:5], 0
	v_mfma_f32_32x32x16_bf16 v[34:49], v[14:17], v[6:9], 0
	ds_read_b128 v[170:173], v219 offset:17936
	s_waitcnt lgkmcnt(7)
	v_mfma_f32_32x32x16_bf16 v[18:33], v[138:141], v[2:5], 0
	ds_read_b64_tr_b16 v[174:175], v220
	ds_read_b64_tr_b16 v[176:177], v220 offset:2304
	v_mfma_f32_32x32x16_bf16 v[2:17], v[138:141], v[6:9], 0
	ds_read_b128 v[138:141], v219 offset:20496
	ds_read_b64_tr_b16 v[154:155], v220 offset:64
	ds_read_b64_tr_b16 v[156:157], v220 offset:2368
	s_waitcnt lgkmcnt(9)
	v_mfma_f32_32x32x16_bf16 v[82:97], v[146:149], v[182:185], v[82:97]
	s_waitcnt vmcnt(6)
	ds_write_b128 v203, v[106:109] offset:30736
	s_and_saveexec_b64 s[12:13], s[4:5]
	ds_write_b128 v216, v[98:101] offset:40976
	s_or_b64 exec, exec, s[12:13]
	s_waitcnt lgkmcnt(8)
	v_mfma_f32_32x32x16_bf16 v[66:81], v[146:149], v[178:181], v[66:81]
	ds_read_b128 v[146:149], v219 offset:15408
	s_waitcnt vmcnt(9)
	v_cvt_pk_bf16_f32 v106, v134, v135
	v_cvt_pk_bf16_f32 v107, v136, v137
	s_waitcnt vmcnt(8)
	v_cvt_pk_bf16_f32 v108, v122, v123
	v_cvt_pk_bf16_f32 v109, v124, v125
	ds_write2_b64 v223, v[106:107], v[108:109] offset1:72
	s_waitcnt vmcnt(7)
	v_cvt_pk_bf16_f32 v106, v150, v151
	v_cvt_pk_bf16_f32 v107, v152, v153
	s_waitcnt vmcnt(6)
	v_cvt_pk_bf16_f32 v108, v142, v143
	v_cvt_pk_bf16_f32 v109, v144, v145
	ds_write2_b64 v223, v[106:107], v[108:109] offset0:144 offset1:216
	v_mfma_f32_32x32x16_bf16 v[50:65], v[158:161], v[182:185], v[50:65]
	global_load_dwordx4 v[106:109], v[200:201], off offset:256
	s_and_saveexec_b64 s[12:13], s[4:5]
	s_cbranch_execz .LBB0_1577
	global_load_dwordx4 v[98:101], v[206:207], off offset:256

; #define G_LOAD(SA, SB, KT) do { SA.load(al, (KT) * 32); SB.load(bl, (KT) * 32); } while (0)
;     __device__ __forceinline__ void prefetch(const AL& al, const BL& bl) {
;         G_LOAD(sa0, sb0, 0);
;         if (1 < nk) G_LOAD(sa1, sb1, 1);
;         if constexpr (BL::DEPTH == 3) { if (2 < nk) G_LOAD(sa2, sb2, 2); }
.LBB0_1613:
	s_or_b64 exec, exec, s[14:15]
	v_add_co_u32_e32 v130, vcc, 0x20000, v214
	s_nop 1
	v_addc_co_u32_e32 v131, vcc, 0, v215, vcc
	v_add_co_u32_e32 v134, vcc, 0x21000, v214
	s_nop 1
	v_addc_co_u32_e32 v135, vcc, 0, v215, vcc
	v_add_co_u32_e32 v138, vcc, 0x22000, v214
	global_load_dwordx4 v[130:133], v[130:131], off
	s_nop 0
	global_load_dwordx4 v[134:137], v[134:135], off
	v_addc_co_u32_e32 v139, vcc, 0, v215, vcc
	v_add_co_u32_e32 v142, vcc, 0x23000, v214
	s_nop 1
	v_addc_co_u32_e32 v143, vcc, 0, v215, vcc
	global_load_dwordx4 v[138:141], v[138:139], off
	s_nop 0
	global_load_dwordx4 v[142:145], v[142:143], off
	v_add_co_u32_e32 v234, vcc, 0x40000, v214
	s_nop 1
	v_addc_co_u32_e32 v235, vcc, 0, v215, vcc
	global_load_dwordx4 v[236:239], v[234:235], off
	v_add_co_u32_e32 v234, vcc, 0x41000, v214
	s_nop 1
	v_addc_co_u32_e32 v235, vcc, 0, v215, vcc
	global_load_dwordx4 v[240:243], v[234:235], off
	v_add_co_u32_e32 v234, vcc, 0x42000, v214
	s_nop 1
	v_addc_co_u32_e32 v235, vcc, 0, v215, vcc
	global_load_dwordx4 v[244:247], v[234:235], off
	v_add_co_u32_e32 v234, vcc, 0x43000, v214
	s_nop 1
	v_addc_co_u32_e32 v235, vcc, 0, v215, vcc
	global_load_dwordx4 v[248:251], v[234:235], off

; #define G_LOAD(SA, SB, KT) do { SA.load(al, (KT) * 32); SB.load(bl, (KT) * 32); } while (0)
;     __device__ __forceinline__ void prefetch(const AL& al, const BL& bl) {
;         G_LOAD(sa0, sb0, 0);
;         if (1 < nk) G_LOAD(sa1, sb1, 1);
;         if constexpr (BL::DEPTH == 3) { if (2 < nk) G_LOAD(sa2, sb2, 2); }
.LBB0_2703:
	s_or_b64 exec, exec, s[6:7]
	v_add_co_u32_e32 v2, vcc, 0x20000, v212
	s_add_i32 s26, 0, 0x21290
	s_nop 0
	v_addc_co_u32_e32 v3, vcc, 0, v213, vcc
	v_add_co_u32_e32 v4, vcc, 0x21000, v212
	s_add_i32 s25, 0, 0x21950
	s_nop 0
	v_addc_co_u32_e32 v5, vcc, 0, v213, vcc
	global_load_dwordx4 v[130:133], v[2:3], off
	global_load_dwordx4 v[134:137], v[4:5], off
	v_add_co_u32_e32 v2, vcc, 0x22000, v212
	s_nop 1
	v_addc_co_u32_e32 v3, vcc, 0, v213, vcc
	v_add_co_u32_e32 v4, vcc, 0x23000, v212
	s_nop 1
	v_addc_co_u32_e32 v5, vcc, 0, v213, vcc
	global_load_dwordx4 v[138:141], v[2:3], off
	global_load_dwordx4 v[142:145], v[4:5], off
	v_add_co_u32_e32 v234, vcc, 0x40000, v212
	s_nop 1
	v_addc_co_u32_e32 v235, vcc, 0, v213, vcc
	global_load_dwordx4 v[236:239], v[234:235], off
	v_add_co_u32_e32 v234, vcc, 0x41000, v212
	s_nop 1
	v_addc_co_u32_e32 v235, vcc, 0, v213, vcc
	global_load_dwordx4 v[240:243], v[234:235], off
	v_add_co_u32_e32 v234, vcc, 0x42000, v212
	s_nop 1
	v_addc_co_u32_e32 v235, vcc, 0, v213, vcc
	global_load_dwordx4 v[244:247], v[234:235], off
	v_add_co_u32_e32 v234, vcc, 0x43000, v212
	s_nop 1
	v_addc_co_u32_e32 v235, vcc, 0, v213, vcc
	global_load_dwordx4 v[248:251], v[234:235], off
	s_andn2_b64 vcc, exec, s[4:5]
	s_cbranch_vccnz .LBB0_2767

; #define G_LOAD(SA, SB, KT) do { SA.load(al, (KT) * 32); SB.load(bl, (KT) * 32); } while (0)
; #define G_STORE(SA, SB, BUF) do { SA.store(As + (BUF) * ASZ, tid); SB.store(Bs3 + (BUF) * BSZ, tid); } while (0)
;     __device__ __forceinline__ void mainloop(bfr* smem, const AL& al, const BL& bl) {
;     ...
;         __syncthreads();
;         G_STORE(sa0, sb0, 0);
;         if (1 < nk) G_STORE(sa1, sb1, 1);
;         if (BL::DEPTH < nk) G_LOAD(sa0, sb0, BL::DEPTH);
;         if (BL::DEPTH + 1 < nk) G_LOAD(sa1, sb1, BL::DEPTH + 1);
;         __builtin_amdgcn_sched_barrier(0);
.LBB0_2712:
	s_or_b64 exec, exec, s[12:13]
	v_add_co_u32_e32 v2, vcc, 0x40000, v212
	s_nop 1
	v_addc_co_u32_e32 v3, vcc, 0, v213, vcc
	v_add_co_u32_e32 v4, vcc, 0x41000, v212
	s_nop 1
	v_addc_co_u32_e32 v5, vcc, 0, v213, vcc
	v_mov_b64_e32 v[134:135], v[236:237]
	v_mov_b64_e32 v[136:137], v[238:239]
	v_mov_b64_e32 v[122:123], v[240:241]
	v_mov_b64_e32 v[124:125], v[242:243]
	v_add_co_u32_e32 v2, vcc, 0x42000, v212
	s_nop 1
	v_addc_co_u32_e32 v3, vcc, 0, v213, vcc
	v_add_co_u32_e32 v4, vcc, 0x43000, v212
	s_nop 1
	v_addc_co_u32_e32 v5, vcc, 0, v213, vcc
	v_mov_b64_e32 v[150:151], v[244:245]
	v_mov_b64_e32 v[152:153], v[246:247]
	v_mov_b64_e32 v[142:143], v[248:249]
	v_mov_b64_e32 v[144:145], v[250:251]
	global_load_dwordx4 v[110:113], v[200:201], off offset:192
	s_and_saveexec_b64 s[12:13], s[4:5]
	s_cbranch_execz .LBB0_2714
	global_load_dwordx4 v[102:105], v[202:203], off offset:192

.Lm2a_ld_18:
	global_load_dword v234, v[248:249], off
	ds_read_b64_tr_b16 v[2:3], v231 offset:46096
	ds_read_b64_tr_b16 v[4:5], v231 offset:48400
	ds_read_b64_tr_b16 v[8:9], v231 offset:48464
	ds_read_b64_tr_b16 v[6:7], v231 offset:46160
	ds_read_b128 v[10:13], v218 offset:16
	ds_read_b128 v[146:149], v218 offset:48
	ds_read_b128 v[14:17], v218 offset:2576
	ds_read_b128 v[158:161], v218 offset:2608
	ds_read_b128 v[138:141], v218 offset:5136
	ds_read_b128 v[162:165], v218 offset:5168
	ds_read_b64_tr_b16 v[182:183], v231 offset:55312
	ds_read_b64_tr_b16 v[184:185], v231 offset:57616
	ds_read_b64_tr_b16 v[180:181], v231 offset:57680
	ds_read_b64_tr_b16 v[178:179], v231 offset:55376
	s_waitcnt lgkmcnt(9)
	v_mfma_f32_32x32x16_bf16 v[82:97], v[10:13], v[2:5], 0
	v_mfma_f32_32x32x16_bf16 v[66:81], v[10:13], v[6:9], 0
	ds_read_b128 v[166:169], v218 offset:15376
	s_waitcnt lgkmcnt(8)
	v_mfma_f32_32x32x16_bf16 v[50:65], v[14:17], v[2:5], 0
	v_mfma_f32_32x32x16_bf16 v[34:49], v[14:17], v[6:9], 0
	ds_read_b128 v[170:173], v218 offset:17936
	s_waitcnt lgkmcnt(7)
	v_mfma_f32_32x32x16_bf16 v[18:33], v[138:141], v[2:5], 0
	ds_read_b64_tr_b16 v[174:175], v219
	ds_read_b64_tr_b16 v[176:177], v219 offset:2304
	v_mfma_f32_32x32x16_bf16 v[2:17], v[138:141], v[6:9], 0
	ds_read_b128 v[138:141], v218 offset:20496
	ds_read_b64_tr_b16 v[154:155], v219 offset:64
	ds_read_b64_tr_b16 v[156:157], v219 offset:2368
	s_waitcnt lgkmcnt(9)
	v_mfma_f32_32x32x16_bf16 v[82:97], v[146:149], v[182:185], v[82:97]
	s_waitcnt vmcnt(6)
	ds_write_b128 v214, v[106:109] offset:30736
	s_and_saveexec_b64 s[12:13], s[4:5]
	ds_write_b128 v215, v[98:101] offset:40976
	s_or_b64 exec, exec, s[12:13]
	s_waitcnt lgkmcnt(8)
	v_mfma_f32_32x32x16_bf16 v[66:81], v[146:149], v[178:181], v[66:81]
	ds_read_b128 v[146:149], v218 offset:15408
	s_waitcnt vmcnt(9)
	v_cvt_pk_bf16_f32 v106, v134, v135
	v_cvt_pk_bf16_f32 v107, v136, v137
	s_waitcnt vmcnt(8)
	v_cvt_pk_bf16_f32 v108, v122, v123
	v_cvt_pk_bf16_f32 v109, v124, v125
	ds_write2_b64 v222, v[106:107], v[108:109] offset1:72
	s_waitcnt vmcnt(7)
	v_cvt_pk_bf16_f32 v106, v150, v151
	v_cvt_pk_bf16_f32 v107, v152, v153
	s_waitcnt vmcnt(6)
	v_cvt_pk_bf16_f32 v108, v142, v143
	v_cvt_pk_bf16_f32 v109, v144, v145
	ds_write2_b64 v222, v[106:107], v[108:109] offset0:144 offset1:216
	v_mfma_f32_32x32x16_bf16 v[50:65], v[158:161], v[182:185], v[50:65]
	global_load_dwordx4 v[106:109], v[200:201], off offset:256
	s_and_saveexec_b64 s[12:13], s[4:5]
	s_cbranch_execz .LBB0_2718
	global_load_dwordx4 v[98:101], v[202:203], off offset:256

; #define G_LOAD(SA, SB, KT) do { SA.load(al, (KT) * 32); SB.load(bl, (KT) * 32); } while (0)
;     __device__ __forceinline__ void prefetch(const AL& al, const BL& bl) {
;         G_LOAD(sa0, sb0, 0);
;         if (1 < nk) G_LOAD(sa1, sb1, 1);
;         if constexpr (BL::DEPTH == 3) { if (2 < nk) G_LOAD(sa2, sb2, 2); }
.LBB0_2754:
	s_or_b64 exec, exec, s[14:15]
	v_add_co_u32_e32 v130, vcc, 0x20000, v212
	s_nop 1
	v_addc_co_u32_e32 v131, vcc, 0, v213, vcc
	v_add_co_u32_e32 v134, vcc, 0x21000, v212
	s_nop 1
	v_addc_co_u32_e32 v135, vcc, 0, v213, vcc
	v_add_co_u32_e32 v138, vcc, 0x22000, v212
	global_load_dwordx4 v[130:133], v[130:131], off
	s_nop 0
	global_load_dwordx4 v[134:137], v[134:135], off
	v_addc_co_u32_e32 v139, vcc, 0, v213, vcc
	v_add_co_u32_e32 v142, vcc, 0x23000, v212
	s_nop 1
	v_addc_co_u32_e32 v143, vcc, 0, v213, vcc
	global_load_dwordx4 v[138:141], v[138:139], off
	s_nop 0
	global_load_dwordx4 v[142:145], v[142:143], off
	v_add_co_u32_e32 v234, vcc, 0x40000, v212
	s_nop 1
	v_addc_co_u32_e32 v235, vcc, 0, v213, vcc
	global_load_dwordx4 v[236:239], v[234:235], off
	v_add_co_u32_e32 v234, vcc, 0x41000, v212
	s_nop 1
	v_addc_co_u32_e32 v235, vcc, 0, v213, vcc
	global_load_dwordx4 v[240:243], v[234:235], off
	v_add_co_u32_e32 v234, vcc, 0x42000, v212
	s_nop 1
	v_addc_co_u32_e32 v235, vcc, 0, v213, vcc
	global_load_dwordx4 v[244:247], v[234:235], off
	v_add_co_u32_e32 v234, vcc, 0x43000, v212
	s_nop 1
	v_addc_co_u32_e32 v235, vcc, 0, v213, vcc
	global_load_dwordx4 v[248:251], v[234:235], off
